# grid barrier: dropped the per-XCD generation increment (nothing waits on it any more) and its completion wait on the XCD-last workgroups
# speedup vs baseline: 1.0299x; 1.0050x over previous
.LBB0_97:
	s_or_b64 exec, exec, s[8:9]
	s_waitcnt vmcnt(0)
	buffer_inv sc1
	s_waitcnt vmcnt(0)
